# U phase: routing gates of the wave's 8 tokens loaded once (coalesced) in the prologue, staged per group in the LDS [slot][token] block and read by ds_read_b32 instead of a per-pair scattered global lo
# baseline (speedup 1.0000x reference)
; #define GAS __attribute__((address_space(1)))
; __device__ __forceinline__ void u_load_grp(UGrp& d, const unsigned char* __restrict__ X1Q, const int* __restrict__ eidx, const float* __restrict__ eus, size_t t0, int lane) {
; #pragma unroll
;     for (int k = 0; k < 4; ++k) { const size_t t = t0 + k; d.xq[k] = *((const GAS v4u*)(X1Q + t * 1024) + lane);
;         const size_t o_lo = ((size_t)(lane >> 4) * 16384 + t) * 16 + (lane & 15), o_hi = o_lo + (size_t)4 * 16384 * 16;
;         d.e_lo[k] = eidx[o_lo]; d.e_hi[k] = eidx[o_hi]; }
; }
; template <int VAR> __device__ __forceinline__ void peer_u_phase(int wave, int grp, int gwl  , LAS unsigned char* lds, gu32* qhead  , const unsigned char* __restrict__ X1Q, const unsigned char* __restrict__ UT, ...
;     ...
;     {
;         gu32* qh = qhead + 64 * grp;
;         (void)qh;
;         const size_t t0 = (size_t)grp * 2048 + (size_t)gwl * 8;
;         UGrp da, db;
;         u_load_grp(da, X1Q, eidx, eus, t0, lane); u_load_grp(db, X1Q, eidx, eus, t0 + 4, lane);
.LBB0_668:
	s_and_b32 s6, s3, -8
	s_add_u32 s18, s8, 0x1e400000
	s_addc_u32 s19, s9, 0
	s_add_u32 s4, s8, 0x15000000
	s_addc_u32 s5, s9, 0
	s_add_u32 s12, s8, 0x14800000
	s_addc_u32 s13, s9, 0
	s_add_u32 s10, s8, 0x19200000
	s_waitcnt vmcnt(0)
	v_mbcnt_lo_u32_b32 v0, -1, 0
	s_addc_u32 s21, s9, 0
	v_mbcnt_hi_u32_b32 v177, -1, v0
	s_lshl_b32 s7, s3, 11
	s_and_b32 s14, s7, 0x3800
	s_add_i32 s6, s6, s61
	v_mov_b32_e32 v136, v177
	s_mul_i32 s7, s61, 0x4800
	s_add_i32 s25, s7, 0
	s_ashr_i32 s7, s6, 31
	v_ashrrev_i32_e32 v138, 4, v136
	s_lshl_b64 s[6:7], s[6:7], 3
	v_ashrrev_i32_e32 v139, 31, v138
	s_add_u32 s14, s6, s14
	v_and_b32_e32 v39, 15, v136
	v_lshlrev_b64 v[0:1], 20, v[138:139]
	s_addc_u32 s17, s7, 0
	v_lshl_add_u64 v[0:1], s[8:9], 0, v[0:1]
	v_lshlrev_b32_e32 v140, 2, v39
	v_mov_b32_e32 v141, 0
	s_mov_b32 s15, s17
	v_lshl_add_u64 v[0:1], v[0:1], 0, v[140:141]
	s_mov_b64 s[26:27], 0x14000000
	v_lshl_add_u64 v[28:29], v[0:1], 0, s[26:27]
	s_lshl_b64 s[26:27], s[14:15], 10
	v_ashrrev_i32_e32 v137, 31, v136
	s_add_u32 s26, s18, s26
	s_addc_u32 s27, s19, s27
	v_lshlrev_b64 v[30:31], 4, v[136:137]
	v_lshl_add_u64 v[4:5], s[26:27], 0, v[30:31]
	s_lshl_b64 s[26:27], s[14:15], 6
	s_or_b32 s16, s14, 1
	v_lshl_add_u64 v[6:7], v[28:29], 0, s[26:27]
	s_mov_b32 s7, 0x400000
	s_lshl_b64 s[26:27], s[16:17], 10
	v_add_co_u32_e32 v8, vcc, s7, v6
	s_add_u32 s26, s18, s26
	s_nop 0
	v_addc_co_u32_e32 v9, vcc, 0, v7, vcc
	s_lshl_b64 s[66:67], s[14:15], 6
	s_add_u32 s66, s66, s12
	s_addc_u32 s67, s67, s13
	s_add_u32 s68, s66, 0x400000
	s_addc_u32 s69, s67, 0
	v_lshlrev_b32_e32 v244, 2, v39
	v_lshl_add_u32 v244, v138, 20, v244
	global_load_dword v236, v244, s[66:67]
	global_load_dword v237, v244, s[66:67] offset:64
	global_load_dword v238, v244, s[66:67] offset:128
	global_load_dword v239, v244, s[66:67] offset:192
	global_load_dword v229, v244, s[66:67] offset:256
	global_load_dword v249, v244, s[66:67] offset:320
	global_load_dword v250, v244, s[66:67] offset:384
	global_load_dword v251, v244, s[66:67] offset:448
	global_load_dword v240, v244, s[68:69]
	global_load_dword v241, v244, s[68:69] offset:64
	global_load_dword v242, v244, s[68:69] offset:128
	global_load_dword v243, v244, s[68:69] offset:192
	global_load_dword v252, v244, s[68:69] offset:256
	global_load_dword v253, v244, s[68:69] offset:320
	global_load_dword v254, v244, s[68:69] offset:384
	global_load_dword v255, v244, s[68:69] offset:448
	global_load_dwordx4 v[0:3], v[4:5], off
	global_load_dword v40, v[6:7], off
	global_load_dword v41, v[8:9], off
	s_addc_u32 s27, s19, s27
	v_lshl_add_u64 v[8:9], s[26:27], 0, v[30:31]
	s_lshl_b64 s[26:27], s[16:17], 6
	v_lshl_add_u64 v[10:11], v[28:29], 0, s[26:27]
	v_add_co_u32_e32 v12, vcc, s7, v10
	s_or_b32 s16, s14, 2
	s_nop 0
	v_addc_co_u32_e32 v13, vcc, 0, v11, vcc
	global_load_dwordx4 v[4:7], v[8:9], off
	global_load_dword v42, v[10:11], off
	global_load_dword v43, v[12:13], off
	s_lshl_b64 s[26:27], s[16:17], 10
	s_add_u32 s26, s18, s26
	s_addc_u32 s27, s19, s27
	v_lshl_add_u64 v[12:13], s[26:27], 0, v[30:31]
	s_lshl_b64 s[26:27], s[16:17], 6
	v_lshl_add_u64 v[14:15], v[28:29], 0, s[26:27]
	v_add_co_u32_e32 v16, vcc, s7, v14
	s_or_b32 s16, s14, 3
	s_nop 0
	v_addc_co_u32_e32 v17, vcc, 0, v15, vcc
	global_load_dwordx4 v[8:11], v[12:13], off
	global_load_dword v44, v[14:15], off
	global_load_dword v45, v[16:17], off
	s_lshl_b64 s[26:27], s[16:17], 10
	s_add_u32 s26, s18, s26
	s_addc_u32 s27, s19, s27
	v_lshl_add_u64 v[16:17], s[26:27], 0, v[30:31]
	s_lshl_b64 s[26:27], s[16:17], 6
	s_or_b32 s16, s14, 4
	v_lshl_add_u64 v[18:19], v[28:29], 0, s[26:27]
	s_lshl_b64 s[26:27], s[16:17], 10
	v_add_co_u32_e32 v20, vcc, s7, v18
	s_add_u32 s26, s18, s26
	s_nop 0
	v_addc_co_u32_e32 v21, vcc, 0, v19, vcc
	global_load_dwordx4 v[12:15], v[16:17], off
	global_load_dword v46, v[18:19], off
	global_load_dword v47, v[20:21], off
	s_addc_u32 s27, s19, s27
	v_lshl_add_u64 v[20:21], s[26:27], 0, v[30:31]
	s_lshl_b64 s[26:27], s[16:17], 6
	v_lshl_add_u64 v[22:23], v[28:29], 0, s[26:27]
	s_or_b32 s26, s14, 5
	s_mov_b32 s27, s17
	s_lshl_b64 s[28:29], s[26:27], 10
	v_add_co_u32_e32 v24, vcc, s7, v22
	s_add_u32 s28, s18, s28
	s_nop 0
	v_addc_co_u32_e32 v25, vcc, 0, v23, vcc
	global_load_dwordx4 v[16:19], v[20:21], off
	global_load_dword v48, v[22:23], off
	global_load_dword v49, v[24:25], off
	s_addc_u32 s29, s19, s29
	s_lshl_b64 s[26:27], s[26:27], 6
	v_lshl_add_u64 v[26:27], v[28:29], 0, s[26:27]
	s_or_b32 s26, s14, 6
	s_mov_b32 s27, s17
	v_lshl_add_u64 v[24:25], s[28:29], 0, v[30:31]
	s_lshl_b64 s[28:29], s[26:27], 10
	v_add_co_u32_e32 v32, vcc, s7, v26
	s_add_u32 s28, s18, s28
	s_nop 0
	v_addc_co_u32_e32 v33, vcc, 0, v27, vcc
	global_load_dwordx4 v[20:23], v[24:25], off
	global_load_dword v50, v[26:27], off
	global_load_dword v51, v[32:33], off
	s_addc_u32 s29, s19, s29
	s_lshl_b64 s[26:27], s[26:27], 6
	v_lshl_add_u64 v[34:35], v[28:29], 0, s[26:27]
	s_or_b32 s26, s14, 7
	s_mov_b32 s27, s17
	v_lshl_add_u64 v[32:33], s[28:29], 0, v[30:31]
	s_lshl_b64 s[28:29], s[26:27], 10
	s_add_u32 s18, s18, s28
	v_add_co_u32_e32 v36, vcc, s7, v34
	s_addc_u32 s19, s19, s29
	s_nop 0
	v_addc_co_u32_e32 v37, vcc, 0, v35, vcc
	global_load_dwordx4 v[24:27], v[32:33], off
	global_load_dword v52, v[34:35], off
	global_load_dword v53, v[36:37], off
	v_lshl_add_u64 v[32:33], s[18:19], 0, v[30:31]
	s_lshl_b64 s[18:19], s[26:27], 6
	v_lshl_add_u64 v[34:35], v[28:29], 0, s[18:19]
	v_add_co_u32_e32 v36, vcc, s7, v34
	v_lshlrev_b32_e32 v142, 4, v136
	s_nop 0
	v_addc_co_u32_e32 v37, vcc, 0, v35, vcc
	global_load_dwordx4 v[28:31], v[32:33], off
	global_load_dword v54, v[34:35], off
	global_load_dword v55, v[36:37], off
; #define LAS __attribute__((address_space(3)))
; template <int VAR> __device__ __forceinline__ void u_process_grp(const UGrp& d, const v4u (&xb)[16], int j, size_t t0, int lane, LAS unsigned char* wl, const unsigned char* __restrict__ UT, const float* __restrict__ egate, unsigned* __restrict__ PW) {
;     const int r = lane & 15, g = lane >> 4;
;     LAS unsigned* list = (LAS unsigned*)(wl + 16384);
;     int n = 0;
; #pragma unroll
;     for (int k = 0; k < 4; ++k) {
;         const bool in_lo = ((d.e_lo[k] >> 11) & 7) == j, in_hi = ((d.e_hi[k] >> 11) & 7) == j;
;         const unsigned long long mlo = __ballot(in_lo), mhi = __ballot(in_hi);
;         const int rk_lo = n + (int)__builtin_amdgcn_mbcnt_hi((unsigned)(mlo >> 32), __builtin_amdgcn_mbcnt_lo((unsigned)mlo, 0u));
;         n += (int)__builtin_popcountll(mlo);
;         const int rk_hi = n + (int)__builtin_amdgcn_mbcnt_hi((unsigned)(mhi >> 32), __builtin_amdgcn_mbcnt_lo((unsigned)mhi, 0u));
;         n += (int)__builtin_popcountll(mhi);
;         if (in_lo) list[rk_lo] = ((unsigned)d.e_lo[k] & 0x3FFFu) | ((unsigned)lane << 14) | ((unsigned)k << 21) | (((unsigned)d.e_lo[k] >> 14) << 24);
;         if (in_hi) list[rk_hi] = ((unsigned)d.e_hi[k] & 0x3FFFu) | ((unsigned)(64 + lane) << 14) | ((unsigned)k << 21) | (((unsigned)d.e_hi[k] >> 14) << 24);
;     }
;     if (n == 0) return;
;     asm volatile("s_waitcnt lgkmcnt(0)" ::: "memory");
;     const size_t blk = t0 >> 6; const int tk0 = (int)(t0 & 63);
;     const unsigned wl_addr = (unsigned)(uintptr_t)wl;
;     ...
;     asm volatile("s_waitcnt lgkmcnt(0)" ::: "memory");
;     U_ISSUE(0);
; #pragma unroll 1
;     for (int s0 = 0; s0 < n; s0 += 64) {
;         const int pl = s0 + lane; const unsigned ent = list[pl < n ? pl : 0];
;         const unsigned slot = (ent >> 14) & 127u, tkk = (ent >> 21) & 7u;
;         const float gate = egate[((size_t)(slot >> 4) * 16384 + (t0 + tkk)) * 16 + (slot & 15u)];
;         const int cl = lane >> 4, src = (int)tkk + 16 * (r >> 2), sel = r & 3;
;         float dv = 0.f;
	v_lshlrev_b32_e32 v32, 10, v136
	v_and_b32_e32 v32, 0xc00, v32
	v_add_u32_e32 v34, s25, v32
	v_xor_b32_e32 v32, 16, v142
	v_ashrrev_i32_e32 v33, 31, v32
	v_lshl_add_u64 v[146:147], s[4:5], 0, v[32:33]
	v_xor_b32_e32 v32, 32, v142
	v_ashrrev_i32_e32 v33, 31, v32
	v_lshl_add_u64 v[148:149], s[4:5], 0, v[32:33]
	v_xor_b32_e32 v32, 48, v142
	v_ashrrev_i32_e32 v33, 31, v32
	v_lshl_add_u64 v[150:151], s[4:5], 0, v[32:33]
	v_xor_b32_e32 v32, 64, v142
	v_ashrrev_i32_e32 v33, 31, v32
	v_lshl_add_u64 v[152:153], s[4:5], 0, v[32:33]
	v_xor_b32_e32 v32, 0x50, v142
	v_ashrrev_i32_e32 v33, 31, v32
	v_lshl_add_u64 v[154:155], s[4:5], 0, v[32:33]
	v_xor_b32_e32 v32, 0x60, v142
	v_ashrrev_i32_e32 v33, 31, v32
	v_lshl_add_u64 v[156:157], s[4:5], 0, v[32:33]
	v_xor_b32_e32 v32, 0x70, v142
	v_ashrrev_i32_e32 v33, 31, v32
	v_lshl_add_u64 v[158:159], s[4:5], 0, v[32:33]
	v_xor_b32_e32 v32, 0x80, v142
	v_ashrrev_i32_e32 v33, 31, v32
	v_lshl_add_u64 v[160:161], s[4:5], 0, v[32:33]
	v_xor_b32_e32 v32, 0x90, v142
	v_ashrrev_i32_e32 v33, 31, v32
	v_lshl_add_u64 v[162:163], s[4:5], 0, v[32:33]
	v_xor_b32_e32 v32, 0xa0, v142
	v_ashrrev_i32_e32 v33, 31, v32
	v_lshl_add_u64 v[164:165], s[4:5], 0, v[32:33]
	v_xor_b32_e32 v32, 0xb0, v142
	v_ashrrev_i32_e32 v33, 31, v32
	v_lshl_add_u64 v[166:167], s[4:5], 0, v[32:33]
	v_xor_b32_e32 v32, 0xc0, v142
	v_ashrrev_i32_e32 v33, 31, v32
	v_lshl_add_u64 v[168:169], s[4:5], 0, v[32:33]
	v_xor_b32_e32 v32, 0xd0, v142
	v_ashrrev_i32_e32 v33, 31, v32
	v_lshl_add_u64 v[170:171], s[4:5], 0, v[32:33]
	v_xor_b32_e32 v32, 0xe0, v142
	v_ashrrev_i32_e32 v33, 31, v32
	v_lshl_add_u64 v[172:173], s[4:5], 0, v[32:33]
	v_xor_b32_e32 v32, 0xf0, v142
	v_ashrrev_i32_e32 v33, 31, v32
	v_lshl_add_u64 v[174:175], s[4:5], 0, v[32:33]
	v_and_b32_e32 v33, 0xffffff0, v136
	v_bitop3_b32 v56, v33, v39, 1 bitop3:0x36
	v_lshlrev_b32_e32 v180, 4, v56
	v_bitop3_b32 v56, v33, v39, 2 bitop3:0x36
	v_lshlrev_b32_e32 v181, 4, v56
	v_bitop3_b32 v56, v33, v39, 3 bitop3:0x36
	v_lshlrev_b32_e32 v182, 4, v56
	v_bitop3_b32 v56, v33, v39, 4 bitop3:0x36
	v_lshlrev_b32_e32 v183, 4, v56
	v_bitop3_b32 v56, v33, v39, 5 bitop3:0x36
	v_lshlrev_b32_e32 v184, 4, v56
	v_bitop3_b32 v56, v33, v39, 6 bitop3:0x36
	v_lshlrev_b32_e32 v185, 4, v56
	v_bitop3_b32 v56, v33, v39, 7 bitop3:0x36
	v_lshlrev_b32_e32 v186, 4, v56
	v_bitop3_b32 v56, v33, v39, 8 bitop3:0x36
	v_lshlrev_b32_e32 v187, 4, v56
	v_bitop3_b32 v56, v33, v39, 9 bitop3:0x36
	v_lshlrev_b32_e32 v188, 4, v56
	v_bitop3_b32 v56, v33, v39, 10 bitop3:0x36
	v_lshlrev_b32_e32 v189, 4, v56
	v_bitop3_b32 v56, v33, v39, 11 bitop3:0x36
	v_ashrrev_i32_e32 v143, 31, v142
	v_lshlrev_b32_e32 v190, 4, v56
	v_bitop3_b32 v56, v33, v39, 12 bitop3:0x36
	v_lshl_add_u64 v[144:145], s[4:5], 0, v[142:143]
	v_lshl_add_u32 v143, v39, 10, s25
	v_lshlrev_b32_e32 v191, 4, v56
	v_bitop3_b32 v56, v33, v39, 13 bitop3:0x36
	v_bitop3_b32 v39, v33, v39, 14 bitop3:0x36
	v_bitop3_b32 v33, v33, v136, 15 bitop3:0x72
	v_and_b32_e32 v38, 64, v177
	s_lshl_b32 s4, s6, 2
	v_lshlrev_b32_e32 v32, 2, v136
	v_lshlrev_b32_e32 v194, 4, v33
	s_waitcnt vmcnt(22)
	v_lshlrev_b32_e32 v33, 10, v40
	v_lshlrev_b32_e32 v36, 14, v136
	s_and_b32 s4, s4, 0xe0
	v_and_or_b32 v195, v32, 48, v38
	v_and_b32_e32 v32, 0x3fff, v40
	v_and_b32_e32 v33, 0xff000000, v33
	s_add_u32 s18, s10, s4
	v_or3_b32 v198, v32, v33, v36
	s_waitcnt vmcnt(21)
	v_lshlrev_b32_e32 v33, 10, v41
	v_add_u32_e32 v37, 0x100000, v36
	s_addc_u32 s19, s21, 0
	s_lshl_b64 s[26:27], s[14:15], 1
	s_and_b32 s6, s16, 60
	v_and_b32_e32 v32, 0x3fff, v41
	v_and_b32_e32 v33, 0xff000000, v33
	s_and_b32 s15, s27, 0xffffff
	s_and_b32 s27, s26, 0xffffff80
	s_lshl_b32 s6, s6, 2
	v_or3_b32 v199, v32, v33, v37
	s_waitcnt vmcnt(19)
	v_lshlrev_b32_e32 v32, 10, v42
	s_add_u32 s20, s10, s6
	s_movk_i32 s6, 0x3fff
	v_and_b32_e32 v32, 0xff000000, v32
	v_and_or_b32 v32, v42, s6, v32
	s_mov_b32 s10, 0x200000
	v_or3_b32 v202, v32, v36, s10
	s_waitcnt vmcnt(18)
	v_lshlrev_b32_e32 v32, 10, v43
	v_and_b32_e32 v32, 0xff000000, v32
	v_and_or_b32 v32, v43, s6, v32
	v_or3_b32 v203, v32, v37, s10
	s_waitcnt vmcnt(16)
	v_lshlrev_b32_e32 v32, 10, v44
	v_and_b32_e32 v32, 0xff000000, v32
	v_and_or_b32 v32, v44, s6, v32
	v_or3_b32 v206, v32, v36, s7
	s_waitcnt vmcnt(15)
	v_lshlrev_b32_e32 v32, 10, v45
	v_and_b32_e32 v32, 0xff000000, v32
	v_and_or_b32 v32, v45, s6, v32
	v_or3_b32 v207, v32, v37, s7
	s_waitcnt vmcnt(13)
	v_lshlrev_b32_e32 v32, 10, v46
	v_and_b32_e32 v32, 0xff000000, v32
	v_and_or_b32 v32, v46, s6, v32
	s_mov_b32 s22, 0x600000
	v_or3_b32 v210, v32, v36, s22
	s_waitcnt vmcnt(12)
	v_lshlrev_b32_e32 v32, 10, v47
	v_and_b32_e32 v32, 0xff000000, v32
	v_and_or_b32 v32, v47, s6, v32
	s_waitcnt vmcnt(10)
	v_lshlrev_b32_e32 v33, 10, v48
	v_or3_b32 v211, v32, v37, s22
	v_and_b32_e32 v32, 0x3fff, v48
	v_and_b32_e32 v33, 0xff000000, v33
	v_or3_b32 v214, v32, v33, v36
	s_waitcnt vmcnt(9)
	v_lshlrev_b32_e32 v33, 10, v49
	v_and_b32_e32 v32, 0x3fff, v49
	v_and_b32_e32 v33, 0xff000000, v33
	v_or3_b32 v215, v32, v33, v37
	s_waitcnt vmcnt(7)
	v_lshlrev_b32_e32 v32, 10, v50
	v_and_b32_e32 v32, 0xff000000, v32
	v_and_or_b32 v32, v50, s6, v32
	v_or3_b32 v218, v32, v36, s10
	s_waitcnt vmcnt(6)
	v_lshlrev_b32_e32 v32, 10, v51
	v_and_b32_e32 v32, 0xff000000, v32
	v_and_or_b32 v32, v51, s6, v32
	v_or3_b32 v219, v32, v37, s10
	s_waitcnt vmcnt(4)
	v_lshlrev_b32_e32 v32, 10, v52
	v_and_b32_e32 v32, 0xff000000, v32
	v_and_or_b32 v32, v52, s6, v32
	v_or3_b32 v222, v32, v36, s7
	s_waitcnt vmcnt(3)
	v_lshlrev_b32_e32 v32, 10, v53
	v_and_b32_e32 v32, 0xff000000, v32
	v_and_or_b32 v32, v53, s6, v32
	v_or3_b32 v223, v32, v37, s7
	s_waitcnt vmcnt(1)
	v_lshlrev_b32_e32 v32, 10, v54
	v_and_b32_e32 v32, 0xff000000, v32
	v_and_or_b32 v32, v54, s6, v32
	v_or3_b32 v226, v32, v36, s22
	s_waitcnt vmcnt(0)
	v_lshlrev_b32_e32 v32, 10, v55
	v_and_b32_e32 v32, 0xff000000, v32
	v_and_b32_e32 v35, 0xffffff00, v142
	v_and_b32_e32 v139, 3, v136
	v_and_or_b32 v32, v55, s6, v32
	v_add_u32_e32 v137, s25, v142
	v_cmp_eq_u32_e64 s[4:5], 2, v139
	v_lshlrev_b32_e32 v192, 4, v56
	v_lshlrev_b32_e32 v193, 4, v39
	s_addc_u32 s21, s21, 0
	v_bfe_u32 v196, v40, 11, 3
	v_bfe_u32 v197, v41, 11, 3
	v_bfe_u32 v200, v42, 11, 3
	v_bfe_u32 v201, v43, 11, 3
	v_bfe_u32 v204, v44, 11, 3
	v_bfe_u32 v205, v45, 11, 3
	v_bfe_u32 v208, v46, 11, 3
	v_bfe_u32 v209, v47, 11, 3
	v_bfe_u32 v212, v48, 11, 3
	v_bfe_u32 v213, v49, 11, 3
	v_bfe_u32 v216, v50, 11, 3
	v_bfe_u32 v217, v51, 11, 3
	v_bfe_u32 v220, v52, 11, 3
	v_bfe_u32 v221, v53, 11, 3
	v_bfe_u32 v224, v54, 11, 3
	v_bfe_u32 v225, v55, 11, 3
	v_or3_b32 v227, v32, v37, s22
	s_add_i32 s29, s25, 0x4040
	s_mov_b64 s[6:7], 0
	s_mov_b64 s[48:49], -1
	v_add_u32_e32 v228, v34, v35
	s_mov_b32 s22, 0x3e6d3388
	s_mov_b32 s24, 0x3f07dc22
	s_mov_b32 s26, 0x3f35f0e3
	s_mov_b32 s28, 0xbe11a98e
	s_mov_b32 s42, 0x3e027906
	s_mov_b32 s43, 0xfffe0000
	s_mov_b32 s70, 23
	v_mov_b32_e32 v176, 0xbf3a00e3
	s_branch .LBB0_670

; #define LAS __attribute__((address_space(3)))
; template <int VAR> __device__ __forceinline__ void peer_u_phase(int wave, int grp, int gwl  , LAS unsigned char* lds, gu32* qhead  , const unsigned char* __restrict__ X1Q, const unsigned char* __restrict__ UT, ...
;     ...
;         for (int h = 0; h < 2; ++h) {
;             v4u xb[16];
; #pragma unroll
;             for (int k = 0; k < 4; ++k) *((LAS v4u*)(wl + k * 1024) + lane) = h == 0 ? da.xq[k] : db.xq[k];
;             asm volatile("s_waitcnt lgkmcnt(0)" ::: "memory");
; #pragma unroll
;             for (int i = 0; i < 16; ++i) xb[i] = *(const LAS v4u*)(wl + (lane & 3) * 1024 + 256 * (lane >> 4) + 16 * i);
;             asm volatile("s_waitcnt lgkmcnt(0)" ::: "memory");
.LBB0_670:
	s_cmp_eq_u32 s61, 7
	s_cbranch_scc1 .Lgst_skip_0
	v_mov_b32_e32 v126, s61
	v_lshlrev_b32_e32 v125, 4, v136
	v_lshl_add_u32 v125, v126, 11, v125
	v_add_u32_e32 v125, 0x24000, v125
	s_cmp_lg_u64 s[48:49], 0
	s_cbranch_scc0 .Lgst_h1_0
	s_waitcnt vmcnt(0)
	ds_write_b128 v125, v[236:239]
	ds_write_b128 v125, v[240:243] offset:1024
	s_branch .Lgst_skip_0
.Lgst_h1_0:
	ds_write_b32 v125, v229
	ds_write_b32 v125, v249 offset:4
	ds_write_b64 v125, v[250:251] offset:8
	ds_write_b128 v125, v[252:255] offset:1024

; template <int VAR> __device__ __forceinline__ void u_process_grp(const UGrp& d, const v4u (&xb)[16], int j, size_t t0, int lane, LAS unsigned char* wl, const unsigned char* __restrict__ UT, const float* __restrict__ egate, unsigned* __restrict__ PW) {
;     ...
;     for (int s0 = 0; s0 < n; s0 += 64) {
;         const int pl = s0 + lane; const unsigned ent = list[pl < n ? pl : 0];
;         const unsigned slot = (ent >> 14) & 127u, tkk = (ent >> 21) & 7u;
;         const float gate = egate[((size_t)(slot >> 4) * 16384 + (t0 + tkk)) * 16 + (slot & 15u)];
.LBB0_708:
	v_add_u32_e32 v96, s52, v136
	v_cmp_gt_i32_e32 vcc, s51, v96
	s_waitcnt lgkmcnt(2)
	v_mov_b32_e32 v97, s17
	v_mov_b32_e32 v233, 0
	v_cndmask_b32_e32 v96, 0, v96, vcc
	v_lshl_add_u32 v96, v96, 2, s25
	ds_read_b32 v231, v96 offset:16384
	s_mov_b32 s54, s53
	s_mov_b32 s55, 0
	v_mov_b32_e32 v235, v138
	s_waitcnt lgkmcnt(0)
	v_bfe_u32 v178, v231, 21, 3
	s_cmp_eq_u32 s61, 7
	s_cbranch_scc1 .Lgld_0
	v_bfe_u32 v96, v231, 14, 7
	v_lshlrev_b32_e32 v98, 2, v178
	v_lshl_add_u32 v96, v96, 4, v98
	s_lshl_b32 s98, s61, 11
	s_add_i32 s98, s98, 0x24000
	v_add_u32_e32 v96, s98, v96
	ds_read_b32 v232, v96
	s_branch .Lgjoin_0
.Lgld_0:
	v_lshrrev_b32_e32 v96, 4, v231
	v_and_b32_e32 v140, 0x1c000, v96
	v_or_b32_e32 v96, s14, v178
	v_lshl_add_u64 v[96:97], v[96:97], 0, v[140:141]
	v_lshlrev_b64 v[96:97], 6, v[96:97]
	v_lshrrev_b32_e32 v98, 12, v231
	v_lshl_add_u64 v[96:97], s[12:13], 0, v[96:97]
	v_and_b32_e32 v140, 60, v98
	v_lshl_add_u64 v[96:97], v[96:97], 0, v[140:141]
	global_load_dword v232, v[96:97], off
.Lgjoin_0:
	v_or_b32_e32 v96, v178, v195
	v_lshlrev_b32_e32 v234, 2, v96
	s_branch .LBB0_712

; template <int VAR> __device__ __forceinline__ void u_process_grp(const UGrp& d, const v4u (&xb)[16], int j, size_t t0, int lane, LAS unsigned char* wl, const unsigned char* __restrict__ UT, const float* __restrict__ egate, unsigned* __restrict__ PW) {
;     ...
;         dv *= __uint_as_float((ent >> 24) << 23) * 0.125f;
;         const pg8::f32x2 gl = pg8::gelu_pk((pg8::f32x2){dv, dv});
;         const float wv = gl.x * gate;
;         if (VAR != 3 && pl < n) PW[(blk * 128 + slot) * 64 + tk0 + tkk] = (__float_as_uint(wv) & 0xFFFE0000u) | ((ent & 0x3FFFu) << 3);
.LBB0_749:
	s_and_saveexec_b64 s[6:7], vcc
	s_cbranch_execz .LBB0_707
	v_lshlrev_b32_sdwa v96, s70, v231 dst_sel:DWORD dst_unused:UNUSED_PAD src0_sel:DWORD src1_sel:BYTE_3
	v_mul_f32_e32 v96, 0x3e000000, v96
	v_mul_f32_e32 v96, v96, v233
	s_waitcnt lgkmcnt(1)
	v_and_b32_e32 v98, 0x7fffffff, v96
	s_waitcnt lgkmcnt(0)
	v_pk_fma_f32 v[98:99], v[98:99], s[22:23], 1.0 op_sel_hi:[0,0,0]
	v_rcp_f32_e32 v98, v98
	v_rcp_f32_e32 v99, v99
	v_mul_f32_e32 v100, v96, v96
	v_mul_f32_e32 v100, 0xbf38aa3b, v100
	v_exp_f32_e32 v100, v100
	v_pk_fma_f32 v[102:103], v[98:99], s[24:25], v[176:177] op_sel_hi:[1,0,0]
	v_bfe_u32 v97, v231, 14, 7
	v_pk_fma_f32 v[102:103], v[98:99], v[102:103], s[26:27] op_sel_hi:[1,1,0]
	v_cmp_gt_f32_e32 vcc, 0, v96
	v_pk_fma_f32 v[102:103], v[98:99], v[102:103], s[28:29] op_sel_hi:[1,1,0]
	v_lshlrev_b32_e32 v140, 2, v178
	v_pk_fma_f32 v[102:103], v[98:99], v[102:103], s[42:43] op_sel_hi:[1,1,0]
	s_nop 0
	v_pk_mul_f32 v[98:99], v[98:99], v[102:103]
	s_nop 0
	v_pk_mul_f32 v[98:99], v[100:101], v[98:99] op_sel_hi:[0,1]
	v_mul_f32_e32 v100, v96, v98
	v_pk_fma_f32 v[98:99], v[96:97], v[98:99], v[96:97] op_sel_hi:[0,1,1] neg_lo:[1,0,0] neg_hi:[1,0,0]
	v_cndmask_b32_e32 v96, v98, v100, vcc
	v_lshlrev_b32_e32 v98, 3, v231
	s_waitcnt vmcnt(0) lgkmcnt(0)
	v_mul_f32_e32 v96, v232, v96
	v_and_b32_e32 v98, 0x1fff8, v98
	v_and_or_b32 v98, v96, s43, v98
	s_cmp_eq_u32 s61, 7
	s_cbranch_scc1 .Lpwd_0
	s_lshl_b32 s98, s61, 11
	s_add_i32 s98, s98, 0x24000
	v_and_b32_e32 v96, 12, v140
	v_lshl_add_u32 v96, v97, 4, v96
	v_add_u32_e32 v96, s98, v96
	ds_write_b32 v96, v98
	s_branch .LBB0_707

; template <int VAR> __device__ __forceinline__ void u_process_grp(const UGrp& d, const v4u (&xb)[16], int j, size_t t0, int lane, LAS unsigned char* wl, const unsigned char* __restrict__ UT, const float* __restrict__ egate, unsigned* __restrict__ PW) {
;     ...
;     for (int s0 = 0; s0 < n; s0 += 64) {
;         const int pl = s0 + lane; const unsigned ent = list[pl < n ? pl : 0];
;         const unsigned slot = (ent >> 14) & 127u, tkk = (ent >> 21) & 7u;
;         const float gate = egate[((size_t)(slot >> 4) * 16384 + (t0 + tkk)) * 16 + (slot & 15u)];
;         const int cl = lane >> 4, src = (int)tkk + 16 * (r >> 2), sel = r & 3;
.LBB0_788:
	v_add_u32_e32 v96, s52, v136
	v_cmp_gt_i32_e32 vcc, s51, v96
	s_waitcnt vmcnt(0)
	v_mov_b32_e32 v179, v141
	s_waitcnt vmcnt(0)
	v_mov_b32_e32 v232, 0
	v_cndmask_b32_e32 v96, 0, v96, vcc
	v_lshl_add_u32 v96, v96, 2, s25
	ds_read_b32 v231, v96 offset:16384
	s_mov_b32 s54, s53
	s_mov_b32 s55, 0
	v_mov_b32_e32 v234, v138
	s_waitcnt lgkmcnt(0)
	v_bfe_u32 v178, v231, 21, 3
	s_cmp_eq_u32 s61, 7
	s_cbranch_scc1 .Lgld_1
	v_bfe_u32 v96, v231, 14, 7
	v_lshlrev_b32_e32 v98, 2, v178
	v_lshl_add_u32 v96, v96, 4, v98
	s_lshl_b32 s98, s61, 11
	s_add_i32 s98, s98, 0x24000
	v_add_u32_e32 v96, s98, v96
	ds_read_b32 v179, v96
	s_branch .Lgjoin_1
.Lgld_1:
	v_lshrrev_b32_e32 v96, 4, v231
	v_and_b32_e32 v140, 0x1c000, v96
	v_lshl_add_u64 v[96:97], s[16:17], 0, v[178:179]
	v_lshl_add_u64 v[96:97], v[96:97], 0, v[140:141]
	v_lshlrev_b64 v[96:97], 6, v[96:97]
	v_lshrrev_b32_e32 v98, 12, v231
	v_lshl_add_u64 v[96:97], s[12:13], 0, v[96:97]
	v_and_b32_e32 v140, 60, v98
	v_lshl_add_u64 v[96:97], v[96:97], 0, v[140:141]
	global_load_dword v179, v[96:97], off
.Lgjoin_1:
	v_or_b32_e32 v96, v178, v195
	v_lshlrev_b32_e32 v233, 2, v96
	s_branch .LBB0_792

; template <int VAR> __device__ __forceinline__ void u_process_grp(const UGrp& d, const v4u (&xb)[16], int j, size_t t0, int lane, LAS unsigned char* wl, const unsigned char* __restrict__ UT, const float* __restrict__ egate, unsigned* __restrict__ PW) {
;     ...
;         dv *= __uint_as_float((ent >> 24) << 23) * 0.125f;
;         const pg8::f32x2 gl = pg8::gelu_pk((pg8::f32x2){dv, dv});
;         const float wv = gl.x * gate;
;         if (VAR != 3 && pl < n) PW[(blk * 128 + slot) * 64 + tk0 + tkk] = (__float_as_uint(wv) & 0xFFFE0000u) | ((ent & 0x3FFFu) << 3);
.LBB0_829:
	s_and_saveexec_b64 s[6:7], vcc
	s_cbranch_execz .LBB0_787
	v_lshlrev_b32_sdwa v96, s70, v231 dst_sel:DWORD dst_unused:UNUSED_PAD src0_sel:DWORD src1_sel:BYTE_3
	v_mul_f32_e32 v96, 0x3e000000, v96
	v_mul_f32_e32 v96, v96, v232
	s_waitcnt lgkmcnt(1)
	v_and_b32_e32 v98, 0x7fffffff, v96
	s_waitcnt lgkmcnt(0)
	v_pk_fma_f32 v[98:99], v[98:99], s[22:23], 1.0 op_sel_hi:[0,0,0]
	v_rcp_f32_e32 v98, v98
	v_rcp_f32_e32 v99, v99
	v_mul_f32_e32 v100, v96, v96
	v_mul_f32_e32 v100, 0xbf38aa3b, v100
	v_exp_f32_e32 v100, v100
	v_pk_fma_f32 v[102:103], v[98:99], s[24:25], v[176:177] op_sel_hi:[1,0,0]
	v_bfe_u32 v97, v231, 14, 7
	v_pk_fma_f32 v[102:103], v[98:99], v[102:103], s[26:27] op_sel_hi:[1,1,0]
	v_cmp_gt_f32_e32 vcc, 0, v96
	v_pk_fma_f32 v[102:103], v[98:99], v[102:103], s[28:29] op_sel_hi:[1,1,0]
	v_lshlrev_b32_e32 v140, 2, v178
	v_pk_fma_f32 v[102:103], v[98:99], v[102:103], s[42:43] op_sel_hi:[1,1,0]
	s_nop 0
	v_pk_mul_f32 v[98:99], v[98:99], v[102:103]
	s_nop 0
	v_pk_mul_f32 v[98:99], v[100:101], v[98:99] op_sel_hi:[0,1]
	v_mul_f32_e32 v100, v96, v98
	v_pk_fma_f32 v[98:99], v[96:97], v[98:99], v[96:97] op_sel_hi:[0,1,1] neg_lo:[1,0,0] neg_hi:[1,0,0]
	v_cndmask_b32_e32 v96, v98, v100, vcc
	v_lshlrev_b32_e32 v98, 3, v231
	s_waitcnt vmcnt(0) lgkmcnt(0)
	v_mul_f32_e32 v96, v179, v96
	v_and_b32_e32 v98, 0x1fff8, v98
	v_and_or_b32 v98, v96, s43, v98
	s_cmp_eq_u32 s61, 7
	s_cbranch_scc1 .Lpwd_1
	s_lshl_b32 s98, s61, 11
	s_add_i32 s98, s98, 0x24000
	v_and_b32_e32 v96, 12, v140
	v_lshl_add_u32 v96, v97, 4, v96
	v_add_u32_e32 v96, s98, v96
	ds_write_b32 v96, v98
	s_branch .LBB0_787

; __device__ __forceinline__ int mk_lane() { int l_ = (int)__builtin_amdgcn_mbcnt_hi(~0u, __builtin_amdgcn_mbcnt_lo(~0u, 0u)); asm volatile("" : "+v"(l_)); return l_; }
; #define GAS __attribute__((address_space(1)))
; #define LAS __attribute__((address_space(3)))
; __device__ __forceinline__ void u_load_grp(UGrp& d, const unsigned char* __restrict__ X1Q, const int* __restrict__ eidx, const float* __restrict__ eus, size_t t0, int lane) {
; #pragma unroll
;     for (int k = 0; k < 4; ++k) { const size_t t = t0 + k; d.xq[k] = *((const GAS v4u*)(X1Q + t * 1024) + lane);
;         const size_t o_lo = ((size_t)(lane >> 4) * 16384 + t) * 16 + (lane & 15), o_hi = o_lo + (size_t)4 * 16384 * 16;
;         d.e_lo[k] = eidx[o_lo]; d.e_hi[k] = eidx[o_hi]; }
; }
; template <int VAR> __device__ __forceinline__ void peer_u_phase(int wave, int grp, int gwl  , LAS unsigned char* lds, gu32* qhead  , const unsigned char* __restrict__ X1Q, const unsigned char* __restrict__ UT, ...
;     const int lane = mk_lane();
;     LAS unsigned char* wl = lds + wave * U_WAVE_LDS;
;     {
;         gu32* qh = qhead + 64 * grp;
;         (void)qh;
;         const size_t t0 = (size_t)grp * 2048 + (size_t)gwl * 8;
;         UGrp da, db;
;         u_load_grp(da, X1Q, eidx, eus, t0, lane); u_load_grp(db, X1Q, eidx, eus, t0 + 4, lane);
.LBB0_1664:
	s_and_b32 s6, s3, -8
	s_add_u32 s18, s8, 0x1e400000
	s_addc_u32 s19, s9, 0
	s_add_u32 s4, s8, 0x16000000
	s_addc_u32 s5, s9, 0
	s_add_u32 s12, s8, 0x14800000
	s_addc_u32 s13, s9, 0
	s_add_u32 s10, s8, 0x19200000
	s_waitcnt vmcnt(0)
	v_mbcnt_lo_u32_b32 v0, -1, 0
	s_addc_u32 s21, s9, 0
	v_mbcnt_hi_u32_b32 v177, -1, v0
	s_lshl_b32 s7, s3, 11
	s_and_b32 s14, s7, 0x3800
	s_add_i32 s6, s6, s61
	v_mov_b32_e32 v136, v177
	s_mul_i32 s7, s61, 0x4800
	s_add_i32 s25, s7, 0
	s_ashr_i32 s7, s6, 31
	v_ashrrev_i32_e32 v138, 4, v136
	s_lshl_b64 s[6:7], s[6:7], 3
	v_ashrrev_i32_e32 v139, 31, v138
	s_add_u32 s14, s6, s14
	v_and_b32_e32 v39, 15, v136
	v_lshlrev_b64 v[0:1], 20, v[138:139]
	s_addc_u32 s17, s7, 0
	v_lshl_add_u64 v[0:1], s[8:9], 0, v[0:1]
	v_lshlrev_b32_e32 v140, 2, v39
	v_mov_b32_e32 v141, 0
	s_mov_b32 s15, s17
	v_lshl_add_u64 v[0:1], v[0:1], 0, v[140:141]
	s_mov_b64 s[26:27], 0x14000000
	v_lshl_add_u64 v[28:29], v[0:1], 0, s[26:27]
	s_lshl_b64 s[26:27], s[14:15], 10
	v_ashrrev_i32_e32 v137, 31, v136
	s_add_u32 s26, s18, s26
	s_addc_u32 s27, s19, s27
	v_lshlrev_b64 v[30:31], 4, v[136:137]
	v_lshl_add_u64 v[4:5], s[26:27], 0, v[30:31]
	s_lshl_b64 s[26:27], s[14:15], 6
	s_or_b32 s16, s14, 1
	v_lshl_add_u64 v[6:7], v[28:29], 0, s[26:27]
	s_mov_b32 s7, 0x400000
	s_lshl_b64 s[26:27], s[16:17], 10
	v_add_co_u32_e32 v8, vcc, s7, v6
	s_add_u32 s26, s18, s26
	s_nop 0
	v_addc_co_u32_e32 v9, vcc, 0, v7, vcc
	s_lshl_b64 s[66:67], s[14:15], 6
	s_add_u32 s66, s66, s12
	s_addc_u32 s67, s67, s13
	s_add_u32 s68, s66, 0x400000
	s_addc_u32 s69, s67, 0
	v_lshlrev_b32_e32 v244, 2, v39
	v_lshl_add_u32 v244, v138, 20, v244
	global_load_dword v236, v244, s[66:67]
	global_load_dword v237, v244, s[66:67] offset:64
	global_load_dword v238, v244, s[66:67] offset:128
	global_load_dword v239, v244, s[66:67] offset:192
	global_load_dword v229, v244, s[66:67] offset:256
	global_load_dword v249, v244, s[66:67] offset:320
	global_load_dword v250, v244, s[66:67] offset:384
	global_load_dword v251, v244, s[66:67] offset:448
	global_load_dword v240, v244, s[68:69]
	global_load_dword v241, v244, s[68:69] offset:64
	global_load_dword v242, v244, s[68:69] offset:128
	global_load_dword v243, v244, s[68:69] offset:192
	global_load_dword v252, v244, s[68:69] offset:256
	global_load_dword v253, v244, s[68:69] offset:320
	global_load_dword v254, v244, s[68:69] offset:384
	global_load_dword v255, v244, s[68:69] offset:448
	global_load_dwordx4 v[0:3], v[4:5], off
	global_load_dword v40, v[6:7], off
	global_load_dword v41, v[8:9], off
	s_addc_u32 s27, s19, s27
	v_lshl_add_u64 v[8:9], s[26:27], 0, v[30:31]
	s_lshl_b64 s[26:27], s[16:17], 6
	v_lshl_add_u64 v[10:11], v[28:29], 0, s[26:27]
	v_add_co_u32_e32 v12, vcc, s7, v10
	s_or_b32 s16, s14, 2
	s_nop 0
	v_addc_co_u32_e32 v13, vcc, 0, v11, vcc
	global_load_dwordx4 v[4:7], v[8:9], off
	global_load_dword v42, v[10:11], off
	global_load_dword v43, v[12:13], off
	s_lshl_b64 s[26:27], s[16:17], 10
	s_add_u32 s26, s18, s26
	s_addc_u32 s27, s19, s27
	v_lshl_add_u64 v[12:13], s[26:27], 0, v[30:31]
	s_lshl_b64 s[26:27], s[16:17], 6
	v_lshl_add_u64 v[14:15], v[28:29], 0, s[26:27]
	v_add_co_u32_e32 v16, vcc, s7, v14
	s_or_b32 s16, s14, 3
	s_nop 0
	v_addc_co_u32_e32 v17, vcc, 0, v15, vcc
	global_load_dwordx4 v[8:11], v[12:13], off
	global_load_dword v44, v[14:15], off
	global_load_dword v45, v[16:17], off
	s_lshl_b64 s[26:27], s[16:17], 10
	s_add_u32 s26, s18, s26
	s_addc_u32 s27, s19, s27
	v_lshl_add_u64 v[16:17], s[26:27], 0, v[30:31]
	s_lshl_b64 s[26:27], s[16:17], 6
	s_or_b32 s16, s14, 4
	v_lshl_add_u64 v[18:19], v[28:29], 0, s[26:27]
	s_lshl_b64 s[26:27], s[16:17], 10
	v_add_co_u32_e32 v20, vcc, s7, v18
	s_add_u32 s26, s18, s26
	s_nop 0
	v_addc_co_u32_e32 v21, vcc, 0, v19, vcc
	global_load_dwordx4 v[12:15], v[16:17], off
	global_load_dword v46, v[18:19], off
	global_load_dword v47, v[20:21], off
	s_addc_u32 s27, s19, s27
	v_lshl_add_u64 v[20:21], s[26:27], 0, v[30:31]
	s_lshl_b64 s[26:27], s[16:17], 6
	v_lshl_add_u64 v[22:23], v[28:29], 0, s[26:27]
	s_or_b32 s26, s14, 5
	s_mov_b32 s27, s17
	s_lshl_b64 s[28:29], s[26:27], 10
	v_add_co_u32_e32 v24, vcc, s7, v22
	s_add_u32 s28, s18, s28
	s_nop 0
	v_addc_co_u32_e32 v25, vcc, 0, v23, vcc
	global_load_dwordx4 v[16:19], v[20:21], off
	global_load_dword v48, v[22:23], off
	global_load_dword v49, v[24:25], off
	s_addc_u32 s29, s19, s29
	s_lshl_b64 s[26:27], s[26:27], 6
	v_lshl_add_u64 v[26:27], v[28:29], 0, s[26:27]
	s_or_b32 s26, s14, 6
	s_mov_b32 s27, s17
	v_lshl_add_u64 v[24:25], s[28:29], 0, v[30:31]
	s_lshl_b64 s[28:29], s[26:27], 10
	v_add_co_u32_e32 v32, vcc, s7, v26
	s_add_u32 s28, s18, s28
	s_nop 0
	v_addc_co_u32_e32 v33, vcc, 0, v27, vcc
	global_load_dwordx4 v[20:23], v[24:25], off
	global_load_dword v50, v[26:27], off
	global_load_dword v51, v[32:33], off
	s_addc_u32 s29, s19, s29
	s_lshl_b64 s[26:27], s[26:27], 6
	v_lshl_add_u64 v[34:35], v[28:29], 0, s[26:27]
	s_or_b32 s26, s14, 7
	s_mov_b32 s27, s17
	v_lshl_add_u64 v[32:33], s[28:29], 0, v[30:31]
	s_lshl_b64 s[28:29], s[26:27], 10
	s_add_u32 s18, s18, s28
	v_add_co_u32_e32 v36, vcc, s7, v34
	s_addc_u32 s19, s19, s29
	s_nop 0
	v_addc_co_u32_e32 v37, vcc, 0, v35, vcc
	global_load_dwordx4 v[24:27], v[32:33], off
	global_load_dword v52, v[34:35], off
	global_load_dword v53, v[36:37], off
	v_lshl_add_u64 v[32:33], s[18:19], 0, v[30:31]
	s_lshl_b64 s[18:19], s[26:27], 6
	v_lshl_add_u64 v[34:35], v[28:29], 0, s[18:19]
	v_add_co_u32_e32 v36, vcc, s7, v34
	v_lshlrev_b32_e32 v142, 4, v136
	s_nop 0
	v_addc_co_u32_e32 v37, vcc, 0, v35, vcc
	global_load_dwordx4 v[28:31], v[32:33], off
	global_load_dword v54, v[34:35], off
; template <int VAR> __device__ __forceinline__ void u_process_grp(const UGrp& d, const v4u (&xb)[16], int j, size_t t0, int lane, LAS unsigned char* wl, const unsigned char* __restrict__ UT, const float* __restrict__ egate, unsigned* __restrict__ PW) {
;     ...
;         const bool in_lo = ((d.e_lo[k] >> 11) & 7) == j, in_hi = ((d.e_hi[k] >> 11) & 7) == j;
;         const unsigned long long mlo = __ballot(in_lo), mhi = __ballot(in_hi);
;         const int rk_lo = n + (int)__builtin_amdgcn_mbcnt_hi((unsigned)(mlo >> 32), __builtin_amdgcn_mbcnt_lo((unsigned)mlo, 0u));
;         n += (int)__builtin_popcountll(mlo);
;         const int rk_hi = n + (int)__builtin_amdgcn_mbcnt_hi((unsigned)(mhi >> 32), __builtin_amdgcn_mbcnt_lo((unsigned)mhi, 0u));
;         n += (int)__builtin_popcountll(mhi);
;         if (in_lo) list[rk_lo] = ((unsigned)d.e_lo[k] & 0x3FFFu) | ((unsigned)lane << 14) | ((unsigned)k << 21) | (((unsigned)d.e_lo[k] >> 14) << 24);
;         if (in_hi) list[rk_hi] = ((unsigned)d.e_hi[k] & 0x3FFFu) | ((unsigned)(64 + lane) << 14) | ((unsigned)k << 21) | (((unsigned)d.e_hi[k] >> 14) << 24);
;     }
;     if (n == 0) return;
;     asm volatile("s_waitcnt lgkmcnt(0)" ::: "memory");
;     const size_t blk = t0 >> 6; const int tk0 = (int)(t0 & 63);
;     const unsigned wl_addr = (unsigned)(uintptr_t)wl;
	global_load_dword v55, v[36:37], off
	v_lshlrev_b32_e32 v32, 10, v136
	v_and_b32_e32 v32, 0xc00, v32
	v_add_u32_e32 v34, s25, v32
	v_xor_b32_e32 v32, 16, v142
	v_ashrrev_i32_e32 v33, 31, v32
	v_lshl_add_u64 v[146:147], s[4:5], 0, v[32:33]
	v_xor_b32_e32 v32, 32, v142
	v_ashrrev_i32_e32 v33, 31, v32
	v_lshl_add_u64 v[148:149], s[4:5], 0, v[32:33]
	v_xor_b32_e32 v32, 48, v142
	v_ashrrev_i32_e32 v33, 31, v32
	v_lshl_add_u64 v[150:151], s[4:5], 0, v[32:33]
	v_xor_b32_e32 v32, 64, v142
	v_ashrrev_i32_e32 v33, 31, v32
	v_lshl_add_u64 v[152:153], s[4:5], 0, v[32:33]
	v_xor_b32_e32 v32, 0x50, v142
	v_ashrrev_i32_e32 v33, 31, v32
	v_lshl_add_u64 v[154:155], s[4:5], 0, v[32:33]
	v_xor_b32_e32 v32, 0x60, v142
	v_ashrrev_i32_e32 v33, 31, v32
	v_lshl_add_u64 v[156:157], s[4:5], 0, v[32:33]
	v_xor_b32_e32 v32, 0x70, v142
	v_ashrrev_i32_e32 v33, 31, v32
	v_lshl_add_u64 v[158:159], s[4:5], 0, v[32:33]
	v_xor_b32_e32 v32, 0x80, v142
	v_ashrrev_i32_e32 v33, 31, v32
	v_lshl_add_u64 v[160:161], s[4:5], 0, v[32:33]
	v_xor_b32_e32 v32, 0x90, v142
	v_ashrrev_i32_e32 v33, 31, v32
	v_lshl_add_u64 v[162:163], s[4:5], 0, v[32:33]
	v_xor_b32_e32 v32, 0xa0, v142
	v_ashrrev_i32_e32 v33, 31, v32
	v_lshl_add_u64 v[164:165], s[4:5], 0, v[32:33]
	v_xor_b32_e32 v32, 0xb0, v142
	v_ashrrev_i32_e32 v33, 31, v32
	v_lshl_add_u64 v[166:167], s[4:5], 0, v[32:33]
	v_xor_b32_e32 v32, 0xc0, v142
	v_ashrrev_i32_e32 v33, 31, v32
	v_lshl_add_u64 v[168:169], s[4:5], 0, v[32:33]
	v_xor_b32_e32 v32, 0xd0, v142
	v_ashrrev_i32_e32 v33, 31, v32
	v_lshl_add_u64 v[170:171], s[4:5], 0, v[32:33]
	v_xor_b32_e32 v32, 0xe0, v142
	v_ashrrev_i32_e32 v33, 31, v32
	v_lshl_add_u64 v[172:173], s[4:5], 0, v[32:33]
	v_xor_b32_e32 v32, 0xf0, v142
	v_ashrrev_i32_e32 v33, 31, v32
	v_lshl_add_u64 v[174:175], s[4:5], 0, v[32:33]
	v_and_b32_e32 v33, 0xffffff0, v136
	v_bitop3_b32 v56, v33, v39, 1 bitop3:0x36
	v_lshlrev_b32_e32 v180, 4, v56
	v_bitop3_b32 v56, v33, v39, 2 bitop3:0x36
	v_lshlrev_b32_e32 v181, 4, v56
	v_bitop3_b32 v56, v33, v39, 3 bitop3:0x36
	v_lshlrev_b32_e32 v182, 4, v56
	v_bitop3_b32 v56, v33, v39, 4 bitop3:0x36
	v_lshlrev_b32_e32 v183, 4, v56
	v_bitop3_b32 v56, v33, v39, 5 bitop3:0x36
	v_lshlrev_b32_e32 v184, 4, v56
	v_bitop3_b32 v56, v33, v39, 6 bitop3:0x36
	v_lshlrev_b32_e32 v185, 4, v56
	v_bitop3_b32 v56, v33, v39, 7 bitop3:0x36
	v_lshlrev_b32_e32 v186, 4, v56
	v_bitop3_b32 v56, v33, v39, 8 bitop3:0x36
	v_lshlrev_b32_e32 v187, 4, v56
	v_bitop3_b32 v56, v33, v39, 9 bitop3:0x36
	v_lshlrev_b32_e32 v188, 4, v56
	v_bitop3_b32 v56, v33, v39, 10 bitop3:0x36
	v_lshlrev_b32_e32 v189, 4, v56
	v_bitop3_b32 v56, v33, v39, 11 bitop3:0x36
	v_ashrrev_i32_e32 v143, 31, v142
	v_lshlrev_b32_e32 v190, 4, v56
	v_bitop3_b32 v56, v33, v39, 12 bitop3:0x36
	v_lshl_add_u64 v[144:145], s[4:5], 0, v[142:143]
	v_lshl_add_u32 v143, v39, 10, s25
	v_lshlrev_b32_e32 v191, 4, v56
	v_bitop3_b32 v56, v33, v39, 13 bitop3:0x36
	v_bitop3_b32 v39, v33, v39, 14 bitop3:0x36
	v_bitop3_b32 v33, v33, v136, 15 bitop3:0x72
	v_and_b32_e32 v38, 64, v177
	s_lshl_b32 s4, s6, 2
	v_lshlrev_b32_e32 v32, 2, v136
	v_lshlrev_b32_e32 v194, 4, v33
	s_waitcnt vmcnt(22)
	v_lshlrev_b32_e32 v33, 10, v40
	v_lshlrev_b32_e32 v36, 14, v136
	s_and_b32 s4, s4, 0xe0
	v_and_or_b32 v195, v32, 48, v38
	v_and_b32_e32 v32, 0x3fff, v40
	v_and_b32_e32 v33, 0xff000000, v33
	s_add_u32 s18, s10, s4
	v_or3_b32 v198, v32, v33, v36
	s_waitcnt vmcnt(21)
	v_lshlrev_b32_e32 v33, 10, v41
	v_add_u32_e32 v37, 0x100000, v36
	s_addc_u32 s19, s21, 0
	s_lshl_b64 s[26:27], s[14:15], 1
	s_and_b32 s6, s16, 60
	v_and_b32_e32 v32, 0x3fff, v41
	v_and_b32_e32 v33, 0xff000000, v33
	s_and_b32 s15, s27, 0xffffff
	s_and_b32 s27, s26, 0xffffff80
	s_lshl_b32 s6, s6, 2
	v_or3_b32 v199, v32, v33, v37
	s_waitcnt vmcnt(19)
	v_lshlrev_b32_e32 v32, 10, v42
	s_add_u32 s20, s10, s6
	s_movk_i32 s6, 0x3fff
	v_and_b32_e32 v32, 0xff000000, v32
	v_and_or_b32 v32, v42, s6, v32
	s_mov_b32 s10, 0x200000
	v_or3_b32 v202, v32, v36, s10
	s_waitcnt vmcnt(18)
	v_lshlrev_b32_e32 v32, 10, v43
	v_and_b32_e32 v32, 0xff000000, v32
	v_and_or_b32 v32, v43, s6, v32
	v_or3_b32 v203, v32, v37, s10
	s_waitcnt vmcnt(16)
	v_lshlrev_b32_e32 v32, 10, v44
	v_and_b32_e32 v32, 0xff000000, v32
	v_and_or_b32 v32, v44, s6, v32
	v_or3_b32 v206, v32, v36, s7
	s_waitcnt vmcnt(15)
	v_lshlrev_b32_e32 v32, 10, v45
	v_and_b32_e32 v32, 0xff000000, v32
	v_and_or_b32 v32, v45, s6, v32
	v_or3_b32 v207, v32, v37, s7
	s_waitcnt vmcnt(13)
	v_lshlrev_b32_e32 v32, 10, v46
	v_and_b32_e32 v32, 0xff000000, v32
	v_and_or_b32 v32, v46, s6, v32
	s_mov_b32 s22, 0x600000
	v_or3_b32 v210, v32, v36, s22
	s_waitcnt vmcnt(12)
	v_lshlrev_b32_e32 v32, 10, v47
	v_and_b32_e32 v32, 0xff000000, v32
	v_and_or_b32 v32, v47, s6, v32
	s_waitcnt vmcnt(10)
	v_lshlrev_b32_e32 v33, 10, v48
	v_or3_b32 v211, v32, v37, s22
	v_and_b32_e32 v32, 0x3fff, v48
	v_and_b32_e32 v33, 0xff000000, v33
	v_or3_b32 v214, v32, v33, v36
	s_waitcnt vmcnt(9)
	v_lshlrev_b32_e32 v33, 10, v49
	v_and_b32_e32 v32, 0x3fff, v49
	v_and_b32_e32 v33, 0xff000000, v33
	v_or3_b32 v215, v32, v33, v37
	s_waitcnt vmcnt(7)
	v_lshlrev_b32_e32 v32, 10, v50
	v_and_b32_e32 v32, 0xff000000, v32
	v_and_or_b32 v32, v50, s6, v32
	v_or3_b32 v218, v32, v36, s10
	s_waitcnt vmcnt(6)
	v_lshlrev_b32_e32 v32, 10, v51
	v_and_b32_e32 v32, 0xff000000, v32
	v_and_or_b32 v32, v51, s6, v32
	v_or3_b32 v219, v32, v37, s10
	s_waitcnt vmcnt(4)
	v_lshlrev_b32_e32 v32, 10, v52
	v_and_b32_e32 v32, 0xff000000, v32
	v_and_or_b32 v32, v52, s6, v32
	v_or3_b32 v222, v32, v36, s7
	s_waitcnt vmcnt(3)
	v_lshlrev_b32_e32 v32, 10, v53
	v_and_b32_e32 v32, 0xff000000, v32
	v_and_or_b32 v32, v53, s6, v32
	v_or3_b32 v223, v32, v37, s7
	s_waitcnt vmcnt(1)
	v_lshlrev_b32_e32 v32, 10, v54
	v_and_b32_e32 v32, 0xff000000, v32
	v_and_or_b32 v32, v54, s6, v32
	v_or3_b32 v226, v32, v36, s22
	s_waitcnt vmcnt(0)
	v_lshlrev_b32_e32 v32, 10, v55
	v_and_b32_e32 v32, 0xff000000, v32
	v_and_b32_e32 v35, 0xffffff00, v142
	v_and_b32_e32 v139, 3, v136
	v_and_or_b32 v32, v55, s6, v32
	v_add_u32_e32 v137, s25, v142
	v_cmp_eq_u32_e64 s[4:5], 2, v139
	v_lshlrev_b32_e32 v192, 4, v56
	v_lshlrev_b32_e32 v193, 4, v39
	s_addc_u32 s21, s21, 0
	v_bfe_u32 v196, v40, 11, 3
	v_bfe_u32 v197, v41, 11, 3
	v_bfe_u32 v200, v42, 11, 3
	v_bfe_u32 v201, v43, 11, 3
	v_bfe_u32 v204, v44, 11, 3
	v_bfe_u32 v205, v45, 11, 3
	v_bfe_u32 v208, v46, 11, 3
	v_bfe_u32 v209, v47, 11, 3
	v_bfe_u32 v212, v48, 11, 3
	v_bfe_u32 v213, v49, 11, 3
	v_bfe_u32 v216, v50, 11, 3
	v_bfe_u32 v217, v51, 11, 3
	v_bfe_u32 v220, v52, 11, 3
	v_bfe_u32 v221, v53, 11, 3
	v_bfe_u32 v224, v54, 11, 3
	v_bfe_u32 v225, v55, 11, 3
	v_or3_b32 v227, v32, v37, s22
	s_add_i32 s29, s25, 0x4040
	s_mov_b64 s[6:7], 0
	s_mov_b64 s[48:49], -1
	v_add_u32_e32 v228, v34, v35
	s_mov_b32 s22, 0x3e6d3388
	s_mov_b32 s24, 0x3f07dc22
	s_mov_b32 s26, 0x3f35f0e3
	s_mov_b32 s28, 0xbe11a98e
	s_mov_b32 s42, 0x3e027906
	s_mov_b32 s43, 0xfffe0000
	s_mov_b32 s70, 23
	v_mov_b32_e32 v176, 0xbf3a00e3
	s_branch .LBB0_1666
